# first K-tile of every unit peeled with srcC=0 MFMAs, per-unit accumulator zeroing removed (up, down, in-proj fp8 loops), on top of the unit-boundary barrier edit
# speedup vs baseline: 1.0066x; 1.0066x over previous
.LBB0_216:
	s_ashr_i32 s57, s56, 31
	s_lshl_b64 s[60:61], s[56:57], 18
	s_add_u32 s60, s13, s60
	s_addc_u32 s61, s26, s61
	s_and_b64 s[66:67], s[62:63], exec
	s_cselect_b32 s7, s61, s81
	s_cselect_b32 s57, s60, s80
	s_ashr_i32 s59, s58, 31
	s_lshl_b64 s[66:67], s[58:59], 18
	s_add_u32 s66, s27, s66
	s_addc_u32 s67, s34, s67
	s_and_b64 s[82:83], s[62:63], exec
	s_cselect_b32 s59, s67, s79
	s_cselect_b32 vcc_lo, s66, s78
	s_add_u32 vcc_hi, s78, 0x100
	s_addc_u32 s89, s79, 0
	s_mov_b32 s33, -2
.LBB0_217:
	s_cmp_lt_i32 s33, 0
	s_cbranch_scc1 .Lpeel1
	ds_read_b128 v[18:21], v168
	ds_read_b128 v[22:25], v168 offset:1024
	ds_read_b128 v[26:29], v168 offset:2048
	ds_read_b128 v[30:33], v168 offset:3072
	ds_read_b128 v[2:5], v169
	ds_read_b128 v[6:9], v169 offset:1024
	ds_read_b128 v[10:13], v169 offset:2048
	ds_read_b128 v[14:17], v169 offset:3072
	s_add_u32 s78, s80, 0x100
	s_addc_u32 s79, s81, 0
	s_cmp_eq_u32 s33, 4
	s_cselect_b32 s86, s57, s78
	s_cselect_b32 s87, s7, s79
	s_cselect_b32 s84, vcc_lo, vcc_hi
	s_cselect_b32 s85, s59, s89
	s_add_u32 s82, s86, 0x80
	s_addc_u32 s83, s87, 0
	ds_read_b128 v[176:179], v170
	ds_read_b128 v[180:183], v170 offset:1024
	ds_read_b128 v[184:187], v170 offset:2048
	ds_read_b128 v[188:191], v170 offset:3072
	ds_read_b128 v[192:195], v170 offset:4096
	ds_read_b128 v[196:199], v170 offset:5120
	ds_read_b128 v[200:203], v170 offset:6144
	ds_read_b128 v[204:207], v170 offset:7168
	s_add_u32 s80, s80, 0x20080
	s_addc_u32 s81, s81, 0
	s_mov_b32 s29, m0
	s_mov_b32 m0, s91
	s_nop 2
	global_load_lds_dwordx4 v162, s[80:81]
	s_mov_b32 m0, s29
	s_nop 0
	s_mov_b32 s29, m0
	s_mov_b32 m0, s92
	s_nop 2
	global_load_lds_dwordx4 v164, s[80:81]
	s_mov_b32 m0, s29
	s_waitcnt vmcnt(8)
	s_waitcnt lgkmcnt(0)
	s_barrier
	s_setprio 1
	s_waitcnt lgkmcnt(6)
	v_mfma_f32_16x16x128_f8f6f4 v[158:161], v[18:25], v[176:183], v[158:161]
	v_mfma_f32_16x16x128_f8f6f4 v[154:157], v[26:33], v[176:183], v[154:157]
	s_waitcnt lgkmcnt(4)
	v_mfma_f32_16x16x128_f8f6f4 v[146:149], v[18:25], v[184:191], v[146:149]
	v_mfma_f32_16x16x128_f8f6f4 v[138:141], v[26:33], v[184:191], v[138:141]
	s_waitcnt lgkmcnt(2)
	v_mfma_f32_16x16x128_f8f6f4 v[130:133], v[18:25], v[192:199], v[130:133]
	v_mfma_f32_16x16x128_f8f6f4 v[122:125], v[26:33], v[192:199], v[122:125]
	s_waitcnt lgkmcnt(0)
	v_mfma_f32_16x16x128_f8f6f4 v[114:117], v[18:25], v[200:207], v[114:117]
	v_mfma_f32_16x16x128_f8f6f4 v[106:109], v[26:33], v[200:207], v[106:109]
	s_setprio 0
	s_setprio 1
	v_mfma_f32_16x16x128_f8f6f4 v[150:153], v[2:9], v[176:183], v[150:153]
	v_mfma_f32_16x16x128_f8f6f4 v[142:145], v[10:17], v[176:183], v[142:145]
	v_mfma_f32_16x16x128_f8f6f4 v[134:137], v[2:9], v[184:191], v[134:137]
	v_mfma_f32_16x16x128_f8f6f4 v[126:129], v[10:17], v[184:191], v[126:129]
	v_mfma_f32_16x16x128_f8f6f4 v[118:121], v[2:9], v[192:199], v[118:121]
	v_mfma_f32_16x16x128_f8f6f4 v[110:113], v[10:17], v[192:199], v[110:113]
	v_mfma_f32_16x16x128_f8f6f4 v[102:105], v[2:9], v[200:207], v[102:105]
	v_mfma_f32_16x16x128_f8f6f4 v[98:101], v[10:17], v[200:207], v[98:101]
	s_setprio 0
	s_barrier
	ds_read_b128 v[176:179], v170 offset:16384
	ds_read_b128 v[180:183], v170 offset:17408
	ds_read_b128 v[184:187], v170 offset:18432
	ds_read_b128 v[188:191], v170 offset:19456
	ds_read_b128 v[192:195], v170 offset:20480
	ds_read_b128 v[196:199], v170 offset:21504
	ds_read_b128 v[200:203], v170 offset:22528
	ds_read_b128 v[204:207], v170 offset:23552
	s_mov_b32 s29, m0
	s_mov_b32 m0, s36
	s_nop 2
	global_load_lds_dwordx4 v163, s[84:85]
	s_mov_b32 m0, s29
	s_add_u32 s80, s84, 0x20000
	s_mov_b32 s29, m0
	s_mov_b32 m0, s37
	s_nop 2
	global_load_lds_dwordx4 v165, s[84:85]
	s_mov_b32 m0, s29
	s_addc_u32 s81, s85, 0
	s_mov_b32 s29, m0
	s_mov_b32 m0, s55
	s_nop 2
	global_load_lds_dwordx4 v163, s[80:81]
	s_mov_b32 m0, s29
	s_nop 0
	s_mov_b32 s29, m0
	s_mov_b32 m0, s77
	s_nop 2
	global_load_lds_dwordx4 v165, s[80:81]
	s_mov_b32 m0, s29
	s_nop 0
	s_mov_b32 s29, m0
	s_mov_b32 m0, s35
	s_nop 2
	global_load_lds_dwordx4 v162, s[86:87]
	s_mov_b32 m0, s29
	s_nop 0
	s_mov_b32 s29, m0
	s_mov_b32 m0, s88
	s_nop 2
	global_load_lds_dwordx4 v164, s[86:87]
	s_mov_b32 m0, s29
	s_waitcnt vmcnt(8)
	s_waitcnt lgkmcnt(0)
	s_barrier
	s_setprio 1
	s_waitcnt lgkmcnt(6)
	v_mfma_f32_16x16x128_f8f6f4 v[94:97], v[18:25], v[176:183], v[94:97]
	v_mfma_f32_16x16x128_f8f6f4 v[90:93], v[26:33], v[176:183], v[90:93]
	s_waitcnt lgkmcnt(4)
	v_mfma_f32_16x16x128_f8f6f4 v[82:85], v[18:25], v[184:191], v[82:85]
	v_mfma_f32_16x16x128_f8f6f4 v[74:77], v[26:33], v[184:191], v[74:77]
	s_waitcnt lgkmcnt(2)
	v_mfma_f32_16x16x128_f8f6f4 v[66:69], v[18:25], v[192:199], v[66:69]
	v_mfma_f32_16x16x128_f8f6f4 v[58:61], v[26:33], v[192:199], v[58:61]
	s_waitcnt lgkmcnt(0)
	v_mfma_f32_16x16x128_f8f6f4 v[50:53], v[18:25], v[200:207], v[50:53]
	v_mfma_f32_16x16x128_f8f6f4 v[42:45], v[26:33], v[200:207], v[42:45]
	s_setprio 0
	s_setprio 1
	v_mfma_f32_16x16x128_f8f6f4 v[86:89], v[2:9], v[176:183], v[86:89]
	v_mfma_f32_16x16x128_f8f6f4 v[78:81], v[10:17], v[176:183], v[78:81]
	v_mfma_f32_16x16x128_f8f6f4 v[70:73], v[2:9], v[184:191], v[70:73]
	v_mfma_f32_16x16x128_f8f6f4 v[62:65], v[10:17], v[184:191], v[62:65]
	v_mfma_f32_16x16x128_f8f6f4 v[54:57], v[2:9], v[192:199], v[54:57]
	v_mfma_f32_16x16x128_f8f6f4 v[46:49], v[10:17], v[192:199], v[46:49]
	v_mfma_f32_16x16x128_f8f6f4 v[38:41], v[2:9], v[200:207], v[38:41]
	v_mfma_f32_16x16x128_f8f6f4 v[34:37], v[10:17], v[200:207], v[34:37]
	s_setprio 0
	s_barrier
.Lmid1:
	ds_read_b128 v[2:5], v172
	ds_read_b128 v[6:9], v172 offset:1024
	ds_read_b128 v[10:13], v172 offset:2048
	ds_read_b128 v[14:17], v172 offset:3072
	ds_read_b128 v[18:21], v174
	ds_read_b128 v[22:25], v174 offset:1024
	ds_read_b128 v[26:29], v174 offset:2048
	ds_read_b128 v[30:33], v174 offset:3072
	ds_read_b128 v[176:179], v170 offset:32768
	ds_read_b128 v[180:183], v170 offset:33792
	ds_read_b128 v[184:187], v170 offset:34816
	ds_read_b128 v[188:191], v170 offset:35840
	ds_read_b128 v[192:195], v170 offset:36864
	ds_read_b128 v[196:199], v170 offset:37888
	ds_read_b128 v[200:203], v170 offset:38912
	ds_read_b128 v[204:207], v170 offset:39936
	s_add_u32 s80, s86, 0x20000
	s_addc_u32 s81, s87, 0
	s_mov_b32 s29, m0
	s_mov_b32 m0, s97
	s_nop 2
	global_load_lds_dwordx4 v162, s[80:81]
	s_mov_b32 m0, s29
	s_nop 0
	s_mov_b32 s29, m0
	s_mov_b32 m0, s3
	s_nop 2
	global_load_lds_dwordx4 v164, s[80:81]
	s_mov_b32 m0, s29
	s_waitcnt vmcnt(8)
	s_waitcnt lgkmcnt(0)
	s_barrier
	s_setprio 1
	s_waitcnt lgkmcnt(6)
	v_mfma_f32_16x16x128_f8f6f4 v[158:161], v[2:9], v[176:183], v[158:161]
	v_mfma_f32_16x16x128_f8f6f4 v[154:157], v[10:17], v[176:183], v[154:157]
	s_waitcnt lgkmcnt(4)
	v_mfma_f32_16x16x128_f8f6f4 v[146:149], v[2:9], v[184:191], v[146:149]
	v_mfma_f32_16x16x128_f8f6f4 v[138:141], v[10:17], v[184:191], v[138:141]
	s_waitcnt lgkmcnt(2)
	v_mfma_f32_16x16x128_f8f6f4 v[130:133], v[2:9], v[192:199], v[130:133]
	v_mfma_f32_16x16x128_f8f6f4 v[122:125], v[10:17], v[192:199], v[122:125]
	s_waitcnt lgkmcnt(0)
	v_mfma_f32_16x16x128_f8f6f4 v[114:117], v[2:9], v[200:207], v[114:117]
	v_mfma_f32_16x16x128_f8f6f4 v[106:109], v[10:17], v[200:207], v[106:109]
	s_setprio 0
	s_setprio 1
	v_mfma_f32_16x16x128_f8f6f4 v[150:153], v[18:25], v[176:183], v[150:153]
	v_mfma_f32_16x16x128_f8f6f4 v[142:145], v[26:33], v[176:183], v[142:145]
	v_mfma_f32_16x16x128_f8f6f4 v[134:137], v[18:25], v[184:191], v[134:137]
	v_mfma_f32_16x16x128_f8f6f4 v[126:129], v[26:33], v[184:191], v[126:129]
	v_mfma_f32_16x16x128_f8f6f4 v[118:121], v[18:25], v[192:199], v[118:121]
	v_mfma_f32_16x16x128_f8f6f4 v[110:113], v[26:33], v[192:199], v[110:113]
	v_mfma_f32_16x16x128_f8f6f4 v[102:105], v[18:25], v[200:207], v[102:105]
	v_mfma_f32_16x16x128_f8f6f4 v[98:101], v[26:33], v[200:207], v[98:101]
	s_setprio 0
	s_barrier
	ds_read_b128 v[176:179], v170 offset:49152
	ds_read_b128 v[180:183], v170 offset:50176
	ds_read_b128 v[184:187], v170 offset:51200
	ds_read_b128 v[188:191], v170 offset:52224
	ds_read_b128 v[192:195], v170 offset:53248
	ds_read_b128 v[196:199], v170 offset:54272
	ds_read_b128 v[200:203], v170 offset:55296
	ds_read_b128 v[204:207], v170 offset:56320
	s_add_u32 s80, s84, 0x80
	s_addc_u32 s81, s85, 0
	s_mov_b32 s29, m0
	s_mov_b32 m0, s90
	s_nop 2
	global_load_lds_dwordx4 v163, s[80:81]
	s_mov_b32 m0, s29
	s_nop 0
	s_mov_b32 s29, m0
	s_mov_b32 m0, s28
	s_nop 2
	global_load_lds_dwordx4 v165, s[80:81]
	s_mov_b32 m0, s29
	s_add_u32 s80, s84, 0x20080
	s_addc_u32 s81, s85, 0
	s_mov_b32 s29, m0
	s_mov_b32 m0, s94
	s_nop 2
	global_load_lds_dwordx4 v163, s[80:81]
	s_mov_b32 m0, s29
	s_nop 0
	s_mov_b32 s29, m0
	s_mov_b32 m0, s95
	s_nop 2
	global_load_lds_dwordx4 v165, s[80:81]
	s_mov_b32 m0, s29
	s_nop 0
	s_mov_b32 s29, m0
	s_mov_b32 m0, s93
	s_nop 2
	global_load_lds_dwordx4 v162, s[82:83]
	s_mov_b32 m0, s29
	s_nop 0
	s_mov_b32 s29, m0
	s_mov_b32 m0, s2
	s_nop 2
	global_load_lds_dwordx4 v164, s[82:83]
	s_mov_b32 m0, s29
	s_waitcnt vmcnt(8)
	s_waitcnt lgkmcnt(0)
	s_barrier
	s_setprio 1
	s_waitcnt lgkmcnt(6)
	v_mfma_f32_16x16x128_f8f6f4 v[94:97], v[2:9], v[176:183], v[94:97]
	v_mfma_f32_16x16x128_f8f6f4 v[90:93], v[10:17], v[176:183], v[90:93]
	s_waitcnt lgkmcnt(4)
	v_mfma_f32_16x16x128_f8f6f4 v[82:85], v[2:9], v[184:191], v[82:85]
	v_mfma_f32_16x16x128_f8f6f4 v[74:77], v[10:17], v[184:191], v[74:77]
	s_waitcnt lgkmcnt(2)
	v_mfma_f32_16x16x128_f8f6f4 v[66:69], v[2:9], v[192:199], v[66:69]
	v_mfma_f32_16x16x128_f8f6f4 v[58:61], v[10:17], v[192:199], v[58:61]
	s_waitcnt lgkmcnt(0)
	v_mfma_f32_16x16x128_f8f6f4 v[50:53], v[2:9], v[200:207], v[50:53]
	v_mfma_f32_16x16x128_f8f6f4 v[42:45], v[10:17], v[200:207], v[42:45]
	s_setprio 0
	s_setprio 1
	v_mfma_f32_16x16x128_f8f6f4 v[86:89], v[18:25], v[176:183], v[86:89]
	v_mfma_f32_16x16x128_f8f6f4 v[78:81], v[26:33], v[176:183], v[78:81]
	v_mfma_f32_16x16x128_f8f6f4 v[70:73], v[18:25], v[184:191], v[70:73]
	v_mfma_f32_16x16x128_f8f6f4 v[62:65], v[26:33], v[184:191], v[62:65]
	v_mfma_f32_16x16x128_f8f6f4 v[54:57], v[18:25], v[192:199], v[54:57]
	v_mfma_f32_16x16x128_f8f6f4 v[46:49], v[26:33], v[192:199], v[46:49]
	v_mfma_f32_16x16x128_f8f6f4 v[38:41], v[18:25], v[200:207], v[38:41]
	v_mfma_f32_16x16x128_f8f6f4 v[34:37], v[26:33], v[200:207], v[34:37]
	s_setprio 0
	s_cmp_lt_i32 s33, 4
	s_cbranch_scc1 .Lkb1_do
	s_cmp_lg_u64 s[10:11], 0
	s_cbranch_scc0 .Lkb1_skip

.Lpeel1:
	ds_read_b128 v[18:21], v168
	ds_read_b128 v[22:25], v168 offset:1024
	ds_read_b128 v[26:29], v168 offset:2048
	ds_read_b128 v[30:33], v168 offset:3072
	ds_read_b128 v[2:5], v169
	ds_read_b128 v[6:9], v169 offset:1024
	ds_read_b128 v[10:13], v169 offset:2048
	ds_read_b128 v[14:17], v169 offset:3072
	s_add_u32 s78, s80, 0x100
	s_addc_u32 s79, s81, 0
	s_cmp_eq_u32 s33, 4
	s_cselect_b32 s86, s57, s78
	s_cselect_b32 s87, s7, s79
	s_cselect_b32 s84, vcc_lo, vcc_hi
	s_cselect_b32 s85, s59, s89
	s_add_u32 s82, s86, 0x80
	s_addc_u32 s83, s87, 0
	ds_read_b128 v[176:179], v170
	ds_read_b128 v[180:183], v170 offset:1024
	ds_read_b128 v[184:187], v170 offset:2048
	ds_read_b128 v[188:191], v170 offset:3072
	ds_read_b128 v[192:195], v170 offset:4096
	ds_read_b128 v[196:199], v170 offset:5120
	ds_read_b128 v[200:203], v170 offset:6144
	ds_read_b128 v[204:207], v170 offset:7168
	s_add_u32 s80, s80, 0x20080
	s_addc_u32 s81, s81, 0
	s_mov_b32 s29, m0
	s_mov_b32 m0, s91
	s_nop 2
	global_load_lds_dwordx4 v162, s[80:81]
	s_mov_b32 m0, s29
	s_nop 0
	s_mov_b32 s29, m0
	s_mov_b32 m0, s92
	s_nop 2
	global_load_lds_dwordx4 v164, s[80:81]
	s_mov_b32 m0, s29
	s_waitcnt vmcnt(8)
	s_waitcnt lgkmcnt(0)
	s_barrier
	s_setprio 1
	s_waitcnt lgkmcnt(6)
	v_mfma_f32_16x16x128_f8f6f4 v[158:161], v[18:25], v[176:183], 0
	v_mfma_f32_16x16x128_f8f6f4 v[154:157], v[26:33], v[176:183], 0
	s_waitcnt lgkmcnt(4)
	v_mfma_f32_16x16x128_f8f6f4 v[146:149], v[18:25], v[184:191], 0
	v_mfma_f32_16x16x128_f8f6f4 v[138:141], v[26:33], v[184:191], 0
	s_waitcnt lgkmcnt(2)
	v_mfma_f32_16x16x128_f8f6f4 v[130:133], v[18:25], v[192:199], 0
	v_mfma_f32_16x16x128_f8f6f4 v[122:125], v[26:33], v[192:199], 0
	s_waitcnt lgkmcnt(0)
	v_mfma_f32_16x16x128_f8f6f4 v[114:117], v[18:25], v[200:207], 0
	v_mfma_f32_16x16x128_f8f6f4 v[106:109], v[26:33], v[200:207], 0
	s_setprio 0
	s_setprio 1
	v_mfma_f32_16x16x128_f8f6f4 v[150:153], v[2:9], v[176:183], 0
	v_mfma_f32_16x16x128_f8f6f4 v[142:145], v[10:17], v[176:183], 0
	v_mfma_f32_16x16x128_f8f6f4 v[134:137], v[2:9], v[184:191], 0
	v_mfma_f32_16x16x128_f8f6f4 v[126:129], v[10:17], v[184:191], 0
	v_mfma_f32_16x16x128_f8f6f4 v[118:121], v[2:9], v[192:199], 0
	v_mfma_f32_16x16x128_f8f6f4 v[110:113], v[10:17], v[192:199], 0
	v_mfma_f32_16x16x128_f8f6f4 v[102:105], v[2:9], v[200:207], 0
	v_mfma_f32_16x16x128_f8f6f4 v[98:101], v[10:17], v[200:207], 0
	s_setprio 0
	s_barrier
	ds_read_b128 v[176:179], v170 offset:16384
	ds_read_b128 v[180:183], v170 offset:17408
	ds_read_b128 v[184:187], v170 offset:18432
	ds_read_b128 v[188:191], v170 offset:19456
	ds_read_b128 v[192:195], v170 offset:20480
	ds_read_b128 v[196:199], v170 offset:21504
	ds_read_b128 v[200:203], v170 offset:22528
	ds_read_b128 v[204:207], v170 offset:23552
	s_mov_b32 s29, m0
	s_mov_b32 m0, s36
	s_nop 2
	global_load_lds_dwordx4 v163, s[84:85]
	s_mov_b32 m0, s29
	s_add_u32 s80, s84, 0x20000
	s_mov_b32 s29, m0
	s_mov_b32 m0, s37
	s_nop 2
	global_load_lds_dwordx4 v165, s[84:85]
	s_mov_b32 m0, s29
	s_addc_u32 s81, s85, 0
	s_mov_b32 s29, m0
	s_mov_b32 m0, s55
	s_nop 2
	global_load_lds_dwordx4 v163, s[80:81]
	s_mov_b32 m0, s29
	s_nop 0
	s_mov_b32 s29, m0
	s_mov_b32 m0, s77
	s_nop 2
	global_load_lds_dwordx4 v165, s[80:81]
	s_mov_b32 m0, s29
	s_nop 0
	s_mov_b32 s29, m0
	s_mov_b32 m0, s35
	s_nop 2
	global_load_lds_dwordx4 v162, s[86:87]
	s_mov_b32 m0, s29
	s_nop 0
	s_mov_b32 s29, m0
	s_mov_b32 m0, s88
	s_nop 2
	global_load_lds_dwordx4 v164, s[86:87]
	s_mov_b32 m0, s29
	s_waitcnt vmcnt(8)
	s_waitcnt lgkmcnt(0)
	s_barrier
	s_setprio 1
	s_waitcnt lgkmcnt(6)
	v_mfma_f32_16x16x128_f8f6f4 v[94:97], v[18:25], v[176:183], 0
	v_mfma_f32_16x16x128_f8f6f4 v[90:93], v[26:33], v[176:183], 0
	s_waitcnt lgkmcnt(4)
	v_mfma_f32_16x16x128_f8f6f4 v[82:85], v[18:25], v[184:191], 0
	v_mfma_f32_16x16x128_f8f6f4 v[74:77], v[26:33], v[184:191], 0
	s_waitcnt lgkmcnt(2)
	v_mfma_f32_16x16x128_f8f6f4 v[66:69], v[18:25], v[192:199], 0
	v_mfma_f32_16x16x128_f8f6f4 v[58:61], v[26:33], v[192:199], 0
	s_waitcnt lgkmcnt(0)
	v_mfma_f32_16x16x128_f8f6f4 v[50:53], v[18:25], v[200:207], 0
	v_mfma_f32_16x16x128_f8f6f4 v[42:45], v[26:33], v[200:207], 0
	s_setprio 0
	s_setprio 1
	v_mfma_f32_16x16x128_f8f6f4 v[86:89], v[2:9], v[176:183], 0
	v_mfma_f32_16x16x128_f8f6f4 v[78:81], v[10:17], v[176:183], 0
	v_mfma_f32_16x16x128_f8f6f4 v[70:73], v[2:9], v[184:191], 0
	v_mfma_f32_16x16x128_f8f6f4 v[62:65], v[10:17], v[184:191], 0
	v_mfma_f32_16x16x128_f8f6f4 v[54:57], v[2:9], v[192:199], 0
	v_mfma_f32_16x16x128_f8f6f4 v[46:49], v[10:17], v[192:199], 0
	v_mfma_f32_16x16x128_f8f6f4 v[38:41], v[2:9], v[200:207], 0
	v_mfma_f32_16x16x128_f8f6f4 v[34:37], v[10:17], v[200:207], 0
	s_setprio 0
	s_barrier
	s_branch .Lmid1

.LBB0_1896:
	s_cmp_eq_u32 s40, 0
	s_cbranch_scc1 .Lpeel6
	s_add_u32 s33, s74, s40
	s_addc_u32 s44, s75, s41
	s_add_u32 s56, s33, 0x1d800080
	s_addc_u32 s57, s44, 0
	s_add_u32 s33, s33, 0x1d800100
	s_addc_u32 s52, s44, 0
	v_add_u32_e32 v2, 0x10000, v173
	v_add_u32_e32 v14, 0x14000, v173
	s_and_b64 s[44:45], s[42:43], exec
	ds_read_b128 v[18:21], v2
	ds_read_b128 v[22:25], v2 offset:1024
	ds_read_b128 v[26:29], v2 offset:2048
	ds_read_b128 v[30:33], v2 offset:3072
	ds_read_b128 v[2:5], v14
	ds_read_b128 v[6:9], v14 offset:1024
	ds_read_b128 v[10:13], v14 offset:2048
	ds_read_b128 v[14:17], v14 offset:3072
	s_cselect_b32 s55, s11, s52
	s_cselect_b32 s54, s10, s33
	s_add_u32 s33, s2, s40
	s_addc_u32 s44, s23, s41
	s_and_b64 s[42:43], s[42:43], exec
	s_cselect_b32 s43, s39, s44
	s_cselect_b32 s42, s38, s33
	s_add_u32 s44, s54, 0x80
	s_addc_u32 s45, s55, 0
	s_add_u32 s52, s42, 0x80
	s_addc_u32 s53, s43, 0
	ds_read_b128 v[180:183], v174
	ds_read_b128 v[184:187], v174 offset:1024
	ds_read_b128 v[188:191], v174 offset:2048
	ds_read_b128 v[192:195], v174 offset:3072
	ds_read_b128 v[196:199], v174 offset:4096
	ds_read_b128 v[200:203], v174 offset:5120
	ds_read_b128 v[204:207], v174 offset:6144
	ds_read_b128 v[208:211], v174 offset:7168
	s_mov_b32 s33, m0
	s_mov_b32 m0, s93
	s_nop 2
	global_load_lds_dwordx4 v178, s[56:57]
	s_mov_b32 m0, s33
	s_nop 0
	s_mov_b32 s33, m0
	s_mov_b32 m0, s94
	s_nop 2
	global_load_lds_dwordx4 v177, s[56:57]
	s_mov_b32 m0, s33
	s_waitcnt vmcnt(8)
	s_waitcnt lgkmcnt(0)
	s_barrier
	s_setprio 1
	s_waitcnt lgkmcnt(6)
	v_mfma_f32_16x16x128_f8f6f4 v[158:161], v[18:25], v[180:187], v[158:161]
	v_mfma_f32_16x16x128_f8f6f4 v[154:157], v[26:33], v[180:187], v[154:157]
	s_waitcnt lgkmcnt(4)
	v_mfma_f32_16x16x128_f8f6f4 v[150:153], v[18:25], v[188:195], v[150:153]
	v_mfma_f32_16x16x128_f8f6f4 v[146:149], v[26:33], v[188:195], v[146:149]
	s_waitcnt lgkmcnt(2)
	v_mfma_f32_16x16x128_f8f6f4 v[142:145], v[18:25], v[196:203], v[142:145]
	v_mfma_f32_16x16x128_f8f6f4 v[138:141], v[26:33], v[196:203], v[138:141]
	s_waitcnt lgkmcnt(0)
	v_mfma_f32_16x16x128_f8f6f4 v[134:137], v[18:25], v[204:211], v[134:137]
	v_mfma_f32_16x16x128_f8f6f4 v[130:133], v[26:33], v[204:211], v[130:133]
	s_setprio 0
	s_setprio 1
	v_mfma_f32_16x16x128_f8f6f4 v[126:129], v[2:9], v[180:187], v[126:129]
	v_mfma_f32_16x16x128_f8f6f4 v[122:125], v[10:17], v[180:187], v[122:125]
	v_mfma_f32_16x16x128_f8f6f4 v[118:121], v[2:9], v[188:195], v[118:121]
	v_mfma_f32_16x16x128_f8f6f4 v[114:117], v[10:17], v[188:195], v[114:117]
	v_mfma_f32_16x16x128_f8f6f4 v[110:113], v[2:9], v[196:203], v[110:113]
	v_mfma_f32_16x16x128_f8f6f4 v[106:109], v[10:17], v[196:203], v[106:109]
	v_mfma_f32_16x16x128_f8f6f4 v[102:105], v[2:9], v[204:211], v[102:105]
	v_mfma_f32_16x16x128_f8f6f4 v[98:101], v[10:17], v[204:211], v[98:101]
	s_setprio 0
	s_barrier
	ds_read_b128 v[180:183], v174 offset:16384
	ds_read_b128 v[184:187], v174 offset:17408
	ds_read_b128 v[188:191], v174 offset:18432
	ds_read_b128 v[192:195], v174 offset:19456
	ds_read_b128 v[196:199], v174 offset:20480
	ds_read_b128 v[200:203], v174 offset:21504
	ds_read_b128 v[204:207], v174 offset:22528
	ds_read_b128 v[208:211], v174 offset:23552
	s_mov_b32 s33, m0
	s_mov_b32 m0, s67
	s_nop 2
	global_load_lds_dwordx4 v1, s[42:43]
	s_mov_b32 m0, s33
	s_add_u32 s56, s42, 0x20000
	s_mov_b32 s33, m0
	s_mov_b32 m0, s68
	s_nop 2
	global_load_lds_dwordx4 v163, s[42:43]
	s_mov_b32 m0, s33
	s_addc_u32 s57, s43, 0
	s_mov_b32 s33, m0
	s_mov_b32 m0, s69
	s_nop 2
	global_load_lds_dwordx4 v1, s[56:57]
	s_mov_b32 m0, s33
	s_nop 0
	s_mov_b32 s33, m0
	s_mov_b32 m0, s76
	s_nop 2
	global_load_lds_dwordx4 v163, s[56:57]
	s_mov_b32 m0, s33
	s_nop 0
	s_mov_b32 s33, m0
	s_mov_b32 m0, s15
	s_nop 2
	global_load_lds_dwordx4 v168, s[54:55]
	s_mov_b32 m0, s33
	s_nop 0
	s_mov_b32 s33, m0
	s_mov_b32 m0, s79
	s_nop 2
	global_load_lds_dwordx4 v172, s[54:55]
	s_mov_b32 m0, s33
	s_waitcnt vmcnt(8)
	s_waitcnt lgkmcnt(0)
	s_barrier
	s_setprio 1
	s_waitcnt lgkmcnt(6)
	v_mfma_f32_16x16x128_f8f6f4 v[94:97], v[18:25], v[180:187], v[94:97]
	v_mfma_f32_16x16x128_f8f6f4 v[90:93], v[26:33], v[180:187], v[90:93]
	s_waitcnt lgkmcnt(4)
	v_mfma_f32_16x16x128_f8f6f4 v[86:89], v[18:25], v[188:195], v[86:89]
	v_mfma_f32_16x16x128_f8f6f4 v[82:85], v[26:33], v[188:195], v[82:85]
	s_waitcnt lgkmcnt(2)
	v_mfma_f32_16x16x128_f8f6f4 v[78:81], v[18:25], v[196:203], v[78:81]
	v_mfma_f32_16x16x128_f8f6f4 v[74:77], v[26:33], v[196:203], v[74:77]
	s_waitcnt lgkmcnt(0)
	v_mfma_f32_16x16x128_f8f6f4 v[70:73], v[18:25], v[204:211], v[70:73]
	v_mfma_f32_16x16x128_f8f6f4 v[66:69], v[26:33], v[204:211], v[66:69]
	s_setprio 0
	s_setprio 1
	v_mfma_f32_16x16x128_f8f6f4 v[62:65], v[2:9], v[180:187], v[62:65]
	v_mfma_f32_16x16x128_f8f6f4 v[58:61], v[10:17], v[180:187], v[58:61]
	v_mfma_f32_16x16x128_f8f6f4 v[54:57], v[2:9], v[188:195], v[54:57]
	v_mfma_f32_16x16x128_f8f6f4 v[50:53], v[10:17], v[188:195], v[50:53]
	v_mfma_f32_16x16x128_f8f6f4 v[46:49], v[2:9], v[196:203], v[46:49]
	v_mfma_f32_16x16x128_f8f6f4 v[42:45], v[10:17], v[196:203], v[42:45]
	v_mfma_f32_16x16x128_f8f6f4 v[38:41], v[2:9], v[204:211], v[38:41]
	v_mfma_f32_16x16x128_f8f6f4 v[34:37], v[10:17], v[204:211], v[34:37]
	s_setprio 0
	s_barrier
.Lmid6:
	v_add_u32_e32 v14, 0x18000, v173
	v_add_u32_e32 v30, 0x1c000, v173
	ds_read_b128 v[2:5], v14
	ds_read_b128 v[6:9], v14 offset:1024
	ds_read_b128 v[10:13], v14 offset:2048
	ds_read_b128 v[14:17], v14 offset:3072
	ds_read_b128 v[18:21], v30
	ds_read_b128 v[22:25], v30 offset:1024
	ds_read_b128 v[26:29], v30 offset:2048
	ds_read_b128 v[30:33], v30 offset:3072
	ds_read_b128 v[180:183], v174 offset:32768
	ds_read_b128 v[184:187], v174 offset:33792
	ds_read_b128 v[188:191], v174 offset:34816
	ds_read_b128 v[192:195], v174 offset:35840
	ds_read_b128 v[196:199], v174 offset:36864
	ds_read_b128 v[200:203], v174 offset:37888
	ds_read_b128 v[204:207], v174 offset:38912
	ds_read_b128 v[208:211], v174 offset:39936
	s_mov_b32 s33, m0
	s_mov_b32 m0, s80
	s_nop 2
	global_load_lds_dwordx4 v169, s[54:55]
	s_mov_b32 m0, s33
	s_nop 0
	s_mov_b32 s33, m0
	s_mov_b32 m0, s81
	s_nop 2
	global_load_lds_dwordx4 v175, s[54:55]
	s_mov_b32 m0, s33
	s_waitcnt vmcnt(8)
	s_waitcnt lgkmcnt(0)
	s_barrier
	s_setprio 1
	s_waitcnt lgkmcnt(6)
	v_mfma_f32_16x16x128_f8f6f4 v[158:161], v[2:9], v[180:187], v[158:161]
	v_mfma_f32_16x16x128_f8f6f4 v[154:157], v[10:17], v[180:187], v[154:157]
	s_waitcnt lgkmcnt(4)
	v_mfma_f32_16x16x128_f8f6f4 v[150:153], v[2:9], v[188:195], v[150:153]
	v_mfma_f32_16x16x128_f8f6f4 v[146:149], v[10:17], v[188:195], v[146:149]
	s_waitcnt lgkmcnt(2)
	v_mfma_f32_16x16x128_f8f6f4 v[142:145], v[2:9], v[196:203], v[142:145]
	v_mfma_f32_16x16x128_f8f6f4 v[138:141], v[10:17], v[196:203], v[138:141]
	s_waitcnt lgkmcnt(0)
	v_mfma_f32_16x16x128_f8f6f4 v[134:137], v[2:9], v[204:211], v[134:137]
	v_mfma_f32_16x16x128_f8f6f4 v[130:133], v[10:17], v[204:211], v[130:133]
	s_setprio 0
	s_setprio 1
	v_mfma_f32_16x16x128_f8f6f4 v[126:129], v[18:25], v[180:187], v[126:129]
	v_mfma_f32_16x16x128_f8f6f4 v[122:125], v[26:33], v[180:187], v[122:125]
	v_mfma_f32_16x16x128_f8f6f4 v[118:121], v[18:25], v[188:195], v[118:121]
	v_mfma_f32_16x16x128_f8f6f4 v[114:117], v[26:33], v[188:195], v[114:117]
	v_mfma_f32_16x16x128_f8f6f4 v[110:113], v[18:25], v[196:203], v[110:113]
	v_mfma_f32_16x16x128_f8f6f4 v[106:109], v[26:33], v[196:203], v[106:109]
	v_mfma_f32_16x16x128_f8f6f4 v[102:105], v[18:25], v[204:211], v[102:105]
	v_mfma_f32_16x16x128_f8f6f4 v[98:101], v[26:33], v[204:211], v[98:101]
	s_setprio 0
	s_barrier
	ds_read_b128 v[180:183], v174 offset:49152
	ds_read_b128 v[184:187], v174 offset:50176
	ds_read_b128 v[188:191], v174 offset:51200
	ds_read_b128 v[192:195], v174 offset:52224
	ds_read_b128 v[196:199], v174 offset:53248
	ds_read_b128 v[200:203], v174 offset:54272
	ds_read_b128 v[204:207], v174 offset:55296
	ds_read_b128 v[208:211], v174 offset:56320
	s_mov_b32 s33, m0
	s_mov_b32 m0, s84
	s_nop 2
	global_load_lds_dwordx4 v1, s[52:53]
	s_mov_b32 m0, s33
	s_add_u32 s42, s42, 0x20080
	s_mov_b32 s33, m0
	s_mov_b32 m0, s85
	s_nop 2
	global_load_lds_dwordx4 v163, s[52:53]
	s_mov_b32 m0, s33
	s_addc_u32 s43, s43, 0
	s_mov_b32 s33, m0
	s_mov_b32 m0, s91
	s_nop 2
	global_load_lds_dwordx4 v1, s[42:43]
	s_mov_b32 m0, s33
	s_nop 0
	s_mov_b32 s33, m0
	s_mov_b32 m0, s92
	s_nop 2
	global_load_lds_dwordx4 v163, s[42:43]
	s_mov_b32 m0, s33
	s_nop 0
	s_mov_b32 s33, m0
	s_mov_b32 m0, s86
	s_nop 2
	global_load_lds_dwordx4 v168, s[44:45]
	s_mov_b32 m0, s33
	s_nop 0
	s_mov_b32 s33, m0
	s_mov_b32 m0, s87
	s_nop 2
	global_load_lds_dwordx4 v172, s[44:45]
	s_mov_b32 m0, s33
	s_waitcnt vmcnt(8)
	s_waitcnt lgkmcnt(0)
	s_barrier
	s_setprio 1
	s_waitcnt lgkmcnt(6)
	v_mfma_f32_16x16x128_f8f6f4 v[94:97], v[2:9], v[180:187], v[94:97]
	v_mfma_f32_16x16x128_f8f6f4 v[90:93], v[10:17], v[180:187], v[90:93]
	s_waitcnt lgkmcnt(4)
	v_mfma_f32_16x16x128_f8f6f4 v[86:89], v[2:9], v[188:195], v[86:89]
	v_mfma_f32_16x16x128_f8f6f4 v[82:85], v[10:17], v[188:195], v[82:85]
	s_waitcnt lgkmcnt(2)
	v_mfma_f32_16x16x128_f8f6f4 v[78:81], v[2:9], v[196:203], v[78:81]
	v_mfma_f32_16x16x128_f8f6f4 v[74:77], v[10:17], v[196:203], v[74:77]
	s_waitcnt lgkmcnt(0)
	v_mfma_f32_16x16x128_f8f6f4 v[70:73], v[2:9], v[204:211], v[70:73]
	v_mfma_f32_16x16x128_f8f6f4 v[66:69], v[10:17], v[204:211], v[66:69]
	s_setprio 0
	s_setprio 1
	v_mfma_f32_16x16x128_f8f6f4 v[62:65], v[18:25], v[180:187], v[62:65]
	v_mfma_f32_16x16x128_f8f6f4 v[58:61], v[26:33], v[180:187], v[58:61]
	v_mfma_f32_16x16x128_f8f6f4 v[54:57], v[18:25], v[188:195], v[54:57]
	v_mfma_f32_16x16x128_f8f6f4 v[50:53], v[26:33], v[188:195], v[50:53]
	v_mfma_f32_16x16x128_f8f6f4 v[46:49], v[18:25], v[196:203], v[46:49]
	v_mfma_f32_16x16x128_f8f6f4 v[42:45], v[26:33], v[196:203], v[42:45]
	v_mfma_f32_16x16x128_f8f6f4 v[38:41], v[18:25], v[204:211], v[38:41]
	v_mfma_f32_16x16x128_f8f6f4 v[34:37], v[26:33], v[204:211], v[34:37]
	s_setprio 0
	s_cmp_lt_i32 s9, 4
	s_cbranch_scc1 .Lkb6_do
	s_cmp_lg_u64 s[16:17], 0
	s_cbranch_scc0 .Lkb6_skip

.Lpeel6:
	s_add_u32 s33, s74, s40
	s_addc_u32 s44, s75, s41
	s_add_u32 s56, s33, 0x1d800080
	s_addc_u32 s57, s44, 0
	s_add_u32 s33, s33, 0x1d800100
	s_addc_u32 s52, s44, 0
	v_add_u32_e32 v2, 0x10000, v173
	v_add_u32_e32 v14, 0x14000, v173
	s_and_b64 s[44:45], s[42:43], exec
	ds_read_b128 v[18:21], v2
	ds_read_b128 v[22:25], v2 offset:1024
	ds_read_b128 v[26:29], v2 offset:2048
	ds_read_b128 v[30:33], v2 offset:3072
	ds_read_b128 v[2:5], v14
	ds_read_b128 v[6:9], v14 offset:1024
	ds_read_b128 v[10:13], v14 offset:2048
	ds_read_b128 v[14:17], v14 offset:3072
	s_cselect_b32 s55, s11, s52
	s_cselect_b32 s54, s10, s33
	s_add_u32 s33, s2, s40
	s_addc_u32 s44, s23, s41
	s_and_b64 s[42:43], s[42:43], exec
	s_cselect_b32 s43, s39, s44
	s_cselect_b32 s42, s38, s33
	s_add_u32 s44, s54, 0x80
	s_addc_u32 s45, s55, 0
	s_add_u32 s52, s42, 0x80
	s_addc_u32 s53, s43, 0
	ds_read_b128 v[180:183], v174
	ds_read_b128 v[184:187], v174 offset:1024
	ds_read_b128 v[188:191], v174 offset:2048
	ds_read_b128 v[192:195], v174 offset:3072
	ds_read_b128 v[196:199], v174 offset:4096
	ds_read_b128 v[200:203], v174 offset:5120
	ds_read_b128 v[204:207], v174 offset:6144
	ds_read_b128 v[208:211], v174 offset:7168
	s_mov_b32 s33, m0
	s_mov_b32 m0, s93
	s_nop 2
	global_load_lds_dwordx4 v178, s[56:57]
	s_mov_b32 m0, s33
	s_nop 0
	s_mov_b32 s33, m0
	s_mov_b32 m0, s94
	s_nop 2
	global_load_lds_dwordx4 v177, s[56:57]
	s_mov_b32 m0, s33
	s_waitcnt vmcnt(8)
	s_waitcnt lgkmcnt(0)
	s_barrier
	s_setprio 1
	s_waitcnt lgkmcnt(6)
	v_mfma_f32_16x16x128_f8f6f4 v[158:161], v[18:25], v[180:187], 0
	v_mfma_f32_16x16x128_f8f6f4 v[154:157], v[26:33], v[180:187], 0
	s_waitcnt lgkmcnt(4)
	v_mfma_f32_16x16x128_f8f6f4 v[150:153], v[18:25], v[188:195], 0
	v_mfma_f32_16x16x128_f8f6f4 v[146:149], v[26:33], v[188:195], 0
	s_waitcnt lgkmcnt(2)
	v_mfma_f32_16x16x128_f8f6f4 v[142:145], v[18:25], v[196:203], 0
	v_mfma_f32_16x16x128_f8f6f4 v[138:141], v[26:33], v[196:203], 0
	s_waitcnt lgkmcnt(0)
	v_mfma_f32_16x16x128_f8f6f4 v[134:137], v[18:25], v[204:211], 0
	v_mfma_f32_16x16x128_f8f6f4 v[130:133], v[26:33], v[204:211], 0
	s_setprio 0
	s_setprio 1
	v_mfma_f32_16x16x128_f8f6f4 v[126:129], v[2:9], v[180:187], 0
	v_mfma_f32_16x16x128_f8f6f4 v[122:125], v[10:17], v[180:187], 0
	v_mfma_f32_16x16x128_f8f6f4 v[118:121], v[2:9], v[188:195], 0
	v_mfma_f32_16x16x128_f8f6f4 v[114:117], v[10:17], v[188:195], 0
	v_mfma_f32_16x16x128_f8f6f4 v[110:113], v[2:9], v[196:203], 0
	v_mfma_f32_16x16x128_f8f6f4 v[106:109], v[10:17], v[196:203], 0
	v_mfma_f32_16x16x128_f8f6f4 v[102:105], v[2:9], v[204:211], 0
	v_mfma_f32_16x16x128_f8f6f4 v[98:101], v[10:17], v[204:211], 0
	s_setprio 0
	s_barrier
	ds_read_b128 v[180:183], v174 offset:16384
	ds_read_b128 v[184:187], v174 offset:17408
	ds_read_b128 v[188:191], v174 offset:18432
	ds_read_b128 v[192:195], v174 offset:19456
	ds_read_b128 v[196:199], v174 offset:20480
	ds_read_b128 v[200:203], v174 offset:21504
	ds_read_b128 v[204:207], v174 offset:22528
	ds_read_b128 v[208:211], v174 offset:23552
	s_mov_b32 s33, m0
	s_mov_b32 m0, s67
	s_nop 2
	global_load_lds_dwordx4 v1, s[42:43]
	s_mov_b32 m0, s33
	s_add_u32 s56, s42, 0x20000
	s_mov_b32 s33, m0
	s_mov_b32 m0, s68
	s_nop 2
	global_load_lds_dwordx4 v163, s[42:43]
	s_mov_b32 m0, s33
	s_addc_u32 s57, s43, 0
	s_mov_b32 s33, m0
	s_mov_b32 m0, s69
	s_nop 2
	global_load_lds_dwordx4 v1, s[56:57]
	s_mov_b32 m0, s33
	s_nop 0
	s_mov_b32 s33, m0
	s_mov_b32 m0, s76
	s_nop 2
	global_load_lds_dwordx4 v163, s[56:57]
	s_mov_b32 m0, s33
	s_nop 0
	s_mov_b32 s33, m0
	s_mov_b32 m0, s15
	s_nop 2
	global_load_lds_dwordx4 v168, s[54:55]
	s_mov_b32 m0, s33
	s_nop 0
	s_mov_b32 s33, m0
	s_mov_b32 m0, s79
	s_nop 2
	global_load_lds_dwordx4 v172, s[54:55]
	s_mov_b32 m0, s33
	s_waitcnt vmcnt(8)
	s_waitcnt lgkmcnt(0)
	s_barrier
	s_setprio 1
	s_waitcnt lgkmcnt(6)
	v_mfma_f32_16x16x128_f8f6f4 v[94:97], v[18:25], v[180:187], 0
	v_mfma_f32_16x16x128_f8f6f4 v[90:93], v[26:33], v[180:187], 0
	s_waitcnt lgkmcnt(4)
	v_mfma_f32_16x16x128_f8f6f4 v[86:89], v[18:25], v[188:195], 0
	v_mfma_f32_16x16x128_f8f6f4 v[82:85], v[26:33], v[188:195], 0
	s_waitcnt lgkmcnt(2)
	v_mfma_f32_16x16x128_f8f6f4 v[78:81], v[18:25], v[196:203], 0
	v_mfma_f32_16x16x128_f8f6f4 v[74:77], v[26:33], v[196:203], 0
	s_waitcnt lgkmcnt(0)
	v_mfma_f32_16x16x128_f8f6f4 v[70:73], v[18:25], v[204:211], 0
	v_mfma_f32_16x16x128_f8f6f4 v[66:69], v[26:33], v[204:211], 0
	s_setprio 0
	s_setprio 1
	v_mfma_f32_16x16x128_f8f6f4 v[62:65], v[2:9], v[180:187], 0
	v_mfma_f32_16x16x128_f8f6f4 v[58:61], v[10:17], v[180:187], 0
	v_mfma_f32_16x16x128_f8f6f4 v[54:57], v[2:9], v[188:195], 0
	v_mfma_f32_16x16x128_f8f6f4 v[50:53], v[10:17], v[188:195], 0
	v_mfma_f32_16x16x128_f8f6f4 v[46:49], v[2:9], v[196:203], 0
	v_mfma_f32_16x16x128_f8f6f4 v[42:45], v[10:17], v[196:203], 0
	v_mfma_f32_16x16x128_f8f6f4 v[38:41], v[2:9], v[204:211], 0
	v_mfma_f32_16x16x128_f8f6f4 v[34:37], v[10:17], v[204:211], 0
	s_setprio 0
	s_barrier
	s_branch .Lmid6

.LBB0_1919:
	v_mov_b32_e32 v177, v175
	v_mov_b32_e32 v178, v169
	s_mov_b32 s30, s36
	s_mov_b32 s36, s65
	s_mov_b32 s14, s22
	s_andn2_b64 vcc, exec, s[26:27]
	s_cbranch_vccnz .LBB0_1921
	s_branch .LBB0_1922

.LBB0_2062:
	s_ashr_i32 s17, s16, 31
	s_lshl_b64 s[20:21], s[16:17], 18
	s_add_u32 s20, s3, s20
	s_addc_u32 s21, s34, s21
	s_and_b64 s[40:41], s[40:41], exec
	s_cselect_b32 s15, s21, s37
	s_cselect_b32 s17, s20, s36
	s_and_b32 s86, s33, 1
	s_lshl_b32 s33, s86, 11
	s_lshl_b32 s38, s38, 8
	s_lshl_b32 s40, s16, 6
	s_add_i32 s33, s33, 0
	s_ashr_i32 s39, s38, 31
	s_ashr_i32 s41, s40, 31
	s_add_i32 s87, s33, 0x21000
	s_add_i32 s88, s33, 0x21400
	s_lshl_b64 s[42:43], s[38:39], 2
	s_add_u32 s89, s50, s42
	s_addc_u32 s90, s51, s43
	s_lshl_b64 s[40:41], s[40:41], 2
	s_add_u32 s40, s60, s40
	s_addc_u32 s41, s61, s41
	s_lshl_b32 s33, s22, 2
	s_add_i32 s39, s33, 0
	s_add_i32 s39, s39, 0x201c0
	s_mov_b32 s91, 0
	s_cmp_eq_u32 s91, 6
	s_cselect_b64 s[42:43], -1, 0
	s_and_b64 vcc, exec, s[6:7]
	s_cbranch_vccnz .LBB0_2084

.LBB0_2092:
	s_cmp_eq_u32 s91, 0
	s_cbranch_scc1 .Lpeel7
	s_lshl_b32 s33, s91, 7
	s_add_u32 s52, s36, s33
	s_addc_u32 s53, s37, 0
	s_add_u32 s46, s52, 0x100
	s_addc_u32 s47, s53, 0
	s_and_b64 s[44:45], s[42:43], exec
	s_cselect_b32 s49, s15, s47
	s_cselect_b32 s48, s17, s46
	s_add_u32 s33, s26, s33
	v_add_u32_e32 v2, 0x10000, v171
	v_add_u32_e32 v14, 0x14000, v171
	s_addc_u32 s44, s27, 0
	ds_read_b128 v[18:21], v2
	ds_read_b128 v[22:25], v2 offset:1024
	ds_read_b128 v[26:29], v2 offset:2048
	ds_read_b128 v[30:33], v2 offset:3072
	ds_read_b128 v[2:5], v14
	ds_read_b128 v[6:9], v14 offset:1024
	ds_read_b128 v[10:13], v14 offset:2048
	ds_read_b128 v[14:17], v14 offset:3072
	s_add_u32 s33, s33, 0x100
	s_addc_u32 s44, s44, 0
	s_and_b64 s[42:43], s[42:43], exec
	s_cselect_b32 s43, s19, s44
	s_cselect_b32 s42, s18, s33
	s_add_u32 s44, s48, 0x80
	s_addc_u32 s45, s49, 0
	s_add_u32 s46, s42, 0x80
	s_addc_u32 s47, s43, 0
	ds_read_b128 v[176:179], v172
	ds_read_b128 v[180:183], v172 offset:1024
	ds_read_b128 v[184:187], v172 offset:2048
	ds_read_b128 v[188:191], v172 offset:3072
	ds_read_b128 v[192:195], v172 offset:4096
	ds_read_b128 v[196:199], v172 offset:5120
	ds_read_b128 v[200:203], v172 offset:6144
	ds_read_b128 v[204:207], v172 offset:7168
	s_add_u32 s52, s52, 0x20080
	s_addc_u32 s53, s53, 0
	s_mov_b32 s33, m0
	s_mov_b32 m0, s79
	s_nop 2
	global_load_lds_dwordx4 v163, s[52:53]
	s_mov_b32 m0, s33
	s_nop 0
	s_mov_b32 s33, m0
	s_mov_b32 m0, s80
	s_nop 2
	global_load_lds_dwordx4 v164, s[52:53]
	s_mov_b32 m0, s33
	s_waitcnt vmcnt(8)
	s_waitcnt lgkmcnt(0)
	s_barrier
	s_setprio 1
	s_waitcnt lgkmcnt(6)
	v_mfma_f32_16x16x128_f8f6f4 v[158:161], v[18:25], v[176:183], v[158:161]
	v_mfma_f32_16x16x128_f8f6f4 v[154:157], v[26:33], v[176:183], v[154:157]
	s_waitcnt lgkmcnt(4)
	v_mfma_f32_16x16x128_f8f6f4 v[142:145], v[18:25], v[184:191], v[142:145]
	v_mfma_f32_16x16x128_f8f6f4 v[138:141], v[26:33], v[184:191], v[138:141]
	s_waitcnt lgkmcnt(2)
	v_mfma_f32_16x16x128_f8f6f4 v[126:129], v[18:25], v[192:199], v[126:129]
	v_mfma_f32_16x16x128_f8f6f4 v[122:125], v[26:33], v[192:199], v[122:125]
	s_waitcnt lgkmcnt(0)
	v_mfma_f32_16x16x128_f8f6f4 v[110:113], v[18:25], v[200:207], v[110:113]
	v_mfma_f32_16x16x128_f8f6f4 v[106:109], v[26:33], v[200:207], v[106:109]
	s_setprio 0
	s_setprio 1
	v_mfma_f32_16x16x128_f8f6f4 v[150:153], v[2:9], v[176:183], v[150:153]
	v_mfma_f32_16x16x128_f8f6f4 v[146:149], v[10:17], v[176:183], v[146:149]
	v_mfma_f32_16x16x128_f8f6f4 v[134:137], v[2:9], v[184:191], v[134:137]
	v_mfma_f32_16x16x128_f8f6f4 v[130:133], v[10:17], v[184:191], v[130:133]
	v_mfma_f32_16x16x128_f8f6f4 v[118:121], v[2:9], v[192:199], v[118:121]
	v_mfma_f32_16x16x128_f8f6f4 v[114:117], v[10:17], v[192:199], v[114:117]
	v_mfma_f32_16x16x128_f8f6f4 v[102:105], v[2:9], v[200:207], v[102:105]
	v_mfma_f32_16x16x128_f8f6f4 v[98:101], v[10:17], v[200:207], v[98:101]
	s_setprio 0
	s_barrier
	ds_read_b128 v[176:179], v172 offset:16384
	ds_read_b128 v[180:183], v172 offset:17408
	ds_read_b128 v[184:187], v172 offset:18432
	ds_read_b128 v[188:191], v172 offset:19456
	ds_read_b128 v[192:195], v172 offset:20480
	ds_read_b128 v[196:199], v172 offset:21504
	ds_read_b128 v[200:203], v172 offset:22528
	ds_read_b128 v[204:207], v172 offset:23552
	s_mov_b32 s33, m0
	s_mov_b32 m0, s64
	s_nop 2
	global_load_lds_dwordx4 v1, s[42:43]
	s_mov_b32 m0, s33
	s_add_u32 s52, s42, 0x20000
	s_mov_b32 s33, m0
	s_mov_b32 m0, s65
	s_nop 2
	global_load_lds_dwordx4 v162, s[42:43]
	s_mov_b32 m0, s33
	s_addc_u32 s53, s43, 0
	s_mov_b32 s33, m0
	s_mov_b32 m0, s24
	s_nop 2
	global_load_lds_dwordx4 v1, s[52:53]
	s_mov_b32 m0, s33
	s_nop 0
	s_mov_b32 s33, m0
	s_mov_b32 m0, s25
	s_nop 2
	global_load_lds_dwordx4 v162, s[52:53]
	s_mov_b32 m0, s33
	s_nop 0
	s_mov_b32 s33, m0
	s_mov_b32 m0, s63
	s_nop 2
	global_load_lds_dwordx4 v163, s[48:49]
	s_mov_b32 m0, s33
	s_nop 0
	s_mov_b32 s33, m0
	s_mov_b32 m0, s2
	s_nop 2
	global_load_lds_dwordx4 v164, s[48:49]
	s_mov_b32 m0, s33
	s_waitcnt vmcnt(8)
	s_waitcnt lgkmcnt(0)
	s_barrier
	s_setprio 1
	s_waitcnt lgkmcnt(6)
	v_mfma_f32_16x16x128_f8f6f4 v[94:97], v[18:25], v[176:183], v[94:97]
	v_mfma_f32_16x16x128_f8f6f4 v[90:93], v[26:33], v[176:183], v[90:93]
	s_waitcnt lgkmcnt(4)
	v_mfma_f32_16x16x128_f8f6f4 v[78:81], v[18:25], v[184:191], v[78:81]
	v_mfma_f32_16x16x128_f8f6f4 v[74:77], v[26:33], v[184:191], v[74:77]
	s_waitcnt lgkmcnt(2)
	v_mfma_f32_16x16x128_f8f6f4 v[62:65], v[18:25], v[192:199], v[62:65]
	v_mfma_f32_16x16x128_f8f6f4 v[58:61], v[26:33], v[192:199], v[58:61]
	s_waitcnt lgkmcnt(0)
	v_mfma_f32_16x16x128_f8f6f4 v[46:49], v[18:25], v[200:207], v[46:49]
	v_mfma_f32_16x16x128_f8f6f4 v[42:45], v[26:33], v[200:207], v[42:45]
	s_setprio 0
	s_setprio 1
	v_mfma_f32_16x16x128_f8f6f4 v[86:89], v[2:9], v[176:183], v[86:89]
	v_mfma_f32_16x16x128_f8f6f4 v[82:85], v[10:17], v[176:183], v[82:85]
	v_mfma_f32_16x16x128_f8f6f4 v[70:73], v[2:9], v[184:191], v[70:73]
	v_mfma_f32_16x16x128_f8f6f4 v[66:69], v[10:17], v[184:191], v[66:69]
	v_mfma_f32_16x16x128_f8f6f4 v[54:57], v[2:9], v[192:199], v[54:57]
	v_mfma_f32_16x16x128_f8f6f4 v[50:53], v[10:17], v[192:199], v[50:53]
	v_mfma_f32_16x16x128_f8f6f4 v[38:41], v[2:9], v[200:207], v[38:41]
	v_mfma_f32_16x16x128_f8f6f4 v[34:37], v[10:17], v[200:207], v[34:37]
	s_setprio 0
	s_barrier
.Lmid7:
	v_add_u32_e32 v14, 0x18000, v171
	v_add_u32_e32 v30, 0x1c000, v171
	ds_read_b128 v[2:5], v14
	ds_read_b128 v[6:9], v14 offset:1024
	ds_read_b128 v[10:13], v14 offset:2048
	ds_read_b128 v[14:17], v14 offset:3072
	ds_read_b128 v[18:21], v30
	ds_read_b128 v[22:25], v30 offset:1024
	ds_read_b128 v[26:29], v30 offset:2048
	ds_read_b128 v[30:33], v30 offset:3072
	ds_read_b128 v[176:179], v172 offset:32768
	ds_read_b128 v[180:183], v172 offset:33792
	ds_read_b128 v[184:187], v172 offset:34816
	ds_read_b128 v[188:191], v172 offset:35840
	ds_read_b128 v[192:195], v172 offset:36864
	ds_read_b128 v[196:199], v172 offset:37888
	ds_read_b128 v[200:203], v172 offset:38912
	ds_read_b128 v[204:207], v172 offset:39936
	s_add_u32 s48, s48, 0x20000
	s_addc_u32 s49, s49, 0
	s_mov_b32 s33, m0
	s_mov_b32 m0, s23
	s_nop 2
	global_load_lds_dwordx4 v163, s[48:49]
	s_mov_b32 m0, s33
	s_nop 0
	s_mov_b32 s33, m0
	s_mov_b32 m0, s28
	s_nop 2
	global_load_lds_dwordx4 v164, s[48:49]
	s_mov_b32 m0, s33
	s_waitcnt vmcnt(8)
	s_waitcnt lgkmcnt(0)
	s_barrier
	s_setprio 1
	s_waitcnt lgkmcnt(6)
	v_mfma_f32_16x16x128_f8f6f4 v[158:161], v[2:9], v[176:183], v[158:161]
	v_mfma_f32_16x16x128_f8f6f4 v[154:157], v[10:17], v[176:183], v[154:157]
	s_waitcnt lgkmcnt(4)
	v_mfma_f32_16x16x128_f8f6f4 v[142:145], v[2:9], v[184:191], v[142:145]
	v_mfma_f32_16x16x128_f8f6f4 v[138:141], v[10:17], v[184:191], v[138:141]
	s_waitcnt lgkmcnt(2)
	v_mfma_f32_16x16x128_f8f6f4 v[126:129], v[2:9], v[192:199], v[126:129]
	v_mfma_f32_16x16x128_f8f6f4 v[122:125], v[10:17], v[192:199], v[122:125]
	s_waitcnt lgkmcnt(0)
	v_mfma_f32_16x16x128_f8f6f4 v[110:113], v[2:9], v[200:207], v[110:113]
	v_mfma_f32_16x16x128_f8f6f4 v[106:109], v[10:17], v[200:207], v[106:109]
	s_setprio 0
	s_setprio 1
	v_mfma_f32_16x16x128_f8f6f4 v[150:153], v[18:25], v[176:183], v[150:153]
	v_mfma_f32_16x16x128_f8f6f4 v[146:149], v[26:33], v[176:183], v[146:149]
	v_mfma_f32_16x16x128_f8f6f4 v[134:137], v[18:25], v[184:191], v[134:137]
	v_mfma_f32_16x16x128_f8f6f4 v[130:133], v[26:33], v[184:191], v[130:133]
	v_mfma_f32_16x16x128_f8f6f4 v[118:121], v[18:25], v[192:199], v[118:121]
	v_mfma_f32_16x16x128_f8f6f4 v[114:117], v[26:33], v[192:199], v[114:117]
	v_mfma_f32_16x16x128_f8f6f4 v[102:105], v[18:25], v[200:207], v[102:105]
	v_mfma_f32_16x16x128_f8f6f4 v[98:101], v[26:33], v[200:207], v[98:101]
	s_setprio 0
	s_barrier
	ds_read_b128 v[176:179], v172 offset:49152
	ds_read_b128 v[180:183], v172 offset:50176
	ds_read_b128 v[184:187], v172 offset:51200
	ds_read_b128 v[188:191], v172 offset:52224
	ds_read_b128 v[192:195], v172 offset:53248
	ds_read_b128 v[196:199], v172 offset:54272
	ds_read_b128 v[200:203], v172 offset:55296
	ds_read_b128 v[204:207], v172 offset:56320
	s_mov_b32 s33, m0
	s_mov_b32 m0, s67
	s_nop 2
	global_load_lds_dwordx4 v1, s[46:47]
	s_mov_b32 m0, s33
	s_add_u32 s42, s42, 0x20080
	s_mov_b32 s33, m0
	s_mov_b32 m0, s68
	s_nop 2
	global_load_lds_dwordx4 v162, s[46:47]
	s_mov_b32 m0, s33
	s_addc_u32 s43, s43, 0
	s_mov_b32 s33, m0
	s_mov_b32 m0, s77
	s_nop 2
	global_load_lds_dwordx4 v1, s[42:43]
	s_mov_b32 m0, s33
	s_nop 0
	s_mov_b32 s33, m0
	s_mov_b32 m0, s78
	s_nop 2
	global_load_lds_dwordx4 v162, s[42:43]
	s_mov_b32 m0, s33
	s_nop 0
	s_mov_b32 s33, m0
	s_mov_b32 m0, s69
	s_nop 2
	global_load_lds_dwordx4 v163, s[44:45]
	s_mov_b32 m0, s33
	s_nop 0
	s_mov_b32 s33, m0
	s_mov_b32 m0, s76
	s_nop 2
	global_load_lds_dwordx4 v164, s[44:45]
	s_mov_b32 m0, s33
	s_waitcnt vmcnt(8)
	s_waitcnt lgkmcnt(0)
	s_barrier
	s_setprio 1
	s_waitcnt lgkmcnt(6)
	v_mfma_f32_16x16x128_f8f6f4 v[94:97], v[2:9], v[176:183], v[94:97]
	v_mfma_f32_16x16x128_f8f6f4 v[90:93], v[10:17], v[176:183], v[90:93]
	s_waitcnt lgkmcnt(4)
	v_mfma_f32_16x16x128_f8f6f4 v[78:81], v[2:9], v[184:191], v[78:81]
	v_mfma_f32_16x16x128_f8f6f4 v[74:77], v[10:17], v[184:191], v[74:77]
	s_waitcnt lgkmcnt(2)
	v_mfma_f32_16x16x128_f8f6f4 v[62:65], v[2:9], v[192:199], v[62:65]
	v_mfma_f32_16x16x128_f8f6f4 v[58:61], v[10:17], v[192:199], v[58:61]
	s_waitcnt lgkmcnt(0)
	v_mfma_f32_16x16x128_f8f6f4 v[46:49], v[2:9], v[200:207], v[46:49]
	v_mfma_f32_16x16x128_f8f6f4 v[42:45], v[10:17], v[200:207], v[42:45]
	s_setprio 0
	s_setprio 1
	v_mfma_f32_16x16x128_f8f6f4 v[86:89], v[18:25], v[176:183], v[86:89]
	v_mfma_f32_16x16x128_f8f6f4 v[82:85], v[26:33], v[176:183], v[82:85]
	v_mfma_f32_16x16x128_f8f6f4 v[70:73], v[18:25], v[184:191], v[70:73]
	v_mfma_f32_16x16x128_f8f6f4 v[66:69], v[26:33], v[184:191], v[66:69]
	v_mfma_f32_16x16x128_f8f6f4 v[54:57], v[18:25], v[192:199], v[54:57]
	v_mfma_f32_16x16x128_f8f6f4 v[50:53], v[26:33], v[192:199], v[50:53]
	v_mfma_f32_16x16x128_f8f6f4 v[38:41], v[18:25], v[200:207], v[38:41]
	v_mfma_f32_16x16x128_f8f6f4 v[34:37], v[26:33], v[200:207], v[34:37]
	s_setprio 0
	s_cmp_lt_u32 s91, 6
	s_cbranch_scc1 .Lkb7_do
	s_cmp_lg_u64 s[12:13], 0
	s_cbranch_scc0 .Lkb7_skip

.Lpeel7:
	s_lshl_b32 s33, s91, 7
	s_add_u32 s52, s36, s33
	s_addc_u32 s53, s37, 0
	s_add_u32 s46, s52, 0x100
	s_addc_u32 s47, s53, 0
	s_and_b64 s[44:45], s[42:43], exec
	s_cselect_b32 s49, s15, s47
	s_cselect_b32 s48, s17, s46
	s_add_u32 s33, s26, s33
	v_add_u32_e32 v2, 0x10000, v171
	v_add_u32_e32 v14, 0x14000, v171
	s_addc_u32 s44, s27, 0
	ds_read_b128 v[18:21], v2
	ds_read_b128 v[22:25], v2 offset:1024
	ds_read_b128 v[26:29], v2 offset:2048
	ds_read_b128 v[30:33], v2 offset:3072
	ds_read_b128 v[2:5], v14
	ds_read_b128 v[6:9], v14 offset:1024
	ds_read_b128 v[10:13], v14 offset:2048
	ds_read_b128 v[14:17], v14 offset:3072
	s_add_u32 s33, s33, 0x100
	s_addc_u32 s44, s44, 0
	s_and_b64 s[42:43], s[42:43], exec
	s_cselect_b32 s43, s19, s44
	s_cselect_b32 s42, s18, s33
	s_add_u32 s44, s48, 0x80
	s_addc_u32 s45, s49, 0
	s_add_u32 s46, s42, 0x80
	s_addc_u32 s47, s43, 0
	ds_read_b128 v[176:179], v172
	ds_read_b128 v[180:183], v172 offset:1024
	ds_read_b128 v[184:187], v172 offset:2048
	ds_read_b128 v[188:191], v172 offset:3072
	ds_read_b128 v[192:195], v172 offset:4096
	ds_read_b128 v[196:199], v172 offset:5120
	ds_read_b128 v[200:203], v172 offset:6144
	ds_read_b128 v[204:207], v172 offset:7168
	s_add_u32 s52, s52, 0x20080
	s_addc_u32 s53, s53, 0
	s_mov_b32 s33, m0
	s_mov_b32 m0, s79
	s_nop 2
	global_load_lds_dwordx4 v163, s[52:53]
	s_mov_b32 m0, s33
	s_nop 0
	s_mov_b32 s33, m0
	s_mov_b32 m0, s80
	s_nop 2
	global_load_lds_dwordx4 v164, s[52:53]
	s_mov_b32 m0, s33
	s_waitcnt vmcnt(8)
	s_waitcnt lgkmcnt(0)
	s_barrier
	s_setprio 1
	s_waitcnt lgkmcnt(6)
	v_mfma_f32_16x16x128_f8f6f4 v[158:161], v[18:25], v[176:183], 0
	v_mfma_f32_16x16x128_f8f6f4 v[154:157], v[26:33], v[176:183], 0
	s_waitcnt lgkmcnt(4)
	v_mfma_f32_16x16x128_f8f6f4 v[142:145], v[18:25], v[184:191], 0
	v_mfma_f32_16x16x128_f8f6f4 v[138:141], v[26:33], v[184:191], 0
	s_waitcnt lgkmcnt(2)
	v_mfma_f32_16x16x128_f8f6f4 v[126:129], v[18:25], v[192:199], 0
	v_mfma_f32_16x16x128_f8f6f4 v[122:125], v[26:33], v[192:199], 0
	s_waitcnt lgkmcnt(0)
	v_mfma_f32_16x16x128_f8f6f4 v[110:113], v[18:25], v[200:207], 0
	v_mfma_f32_16x16x128_f8f6f4 v[106:109], v[26:33], v[200:207], 0
	s_setprio 0
	s_setprio 1
	v_mfma_f32_16x16x128_f8f6f4 v[150:153], v[2:9], v[176:183], 0
	v_mfma_f32_16x16x128_f8f6f4 v[146:149], v[10:17], v[176:183], 0
	v_mfma_f32_16x16x128_f8f6f4 v[134:137], v[2:9], v[184:191], 0
	v_mfma_f32_16x16x128_f8f6f4 v[130:133], v[10:17], v[184:191], 0
	v_mfma_f32_16x16x128_f8f6f4 v[118:121], v[2:9], v[192:199], 0
	v_mfma_f32_16x16x128_f8f6f4 v[114:117], v[10:17], v[192:199], 0
	v_mfma_f32_16x16x128_f8f6f4 v[102:105], v[2:9], v[200:207], 0
	v_mfma_f32_16x16x128_f8f6f4 v[98:101], v[10:17], v[200:207], 0
	s_setprio 0
	s_barrier
	ds_read_b128 v[176:179], v172 offset:16384
	ds_read_b128 v[180:183], v172 offset:17408
	ds_read_b128 v[184:187], v172 offset:18432
	ds_read_b128 v[188:191], v172 offset:19456
	ds_read_b128 v[192:195], v172 offset:20480
	ds_read_b128 v[196:199], v172 offset:21504
	ds_read_b128 v[200:203], v172 offset:22528
	ds_read_b128 v[204:207], v172 offset:23552
	s_mov_b32 s33, m0
	s_mov_b32 m0, s64
	s_nop 2
	global_load_lds_dwordx4 v1, s[42:43]
	s_mov_b32 m0, s33
	s_add_u32 s52, s42, 0x20000
	s_mov_b32 s33, m0
	s_mov_b32 m0, s65
	s_nop 2
	global_load_lds_dwordx4 v162, s[42:43]
	s_mov_b32 m0, s33
	s_addc_u32 s53, s43, 0
	s_mov_b32 s33, m0
	s_mov_b32 m0, s24
	s_nop 2
	global_load_lds_dwordx4 v1, s[52:53]
	s_mov_b32 m0, s33
	s_nop 0
	s_mov_b32 s33, m0
	s_mov_b32 m0, s25
	s_nop 2
	global_load_lds_dwordx4 v162, s[52:53]
	s_mov_b32 m0, s33
	s_nop 0
	s_mov_b32 s33, m0
	s_mov_b32 m0, s63
	s_nop 2
	global_load_lds_dwordx4 v163, s[48:49]
	s_mov_b32 m0, s33
	s_nop 0
	s_mov_b32 s33, m0
	s_mov_b32 m0, s2
	s_nop 2
	global_load_lds_dwordx4 v164, s[48:49]
	s_mov_b32 m0, s33
	s_waitcnt vmcnt(8)
	s_waitcnt lgkmcnt(0)
	s_barrier
	s_setprio 1
	s_waitcnt lgkmcnt(6)
	v_mfma_f32_16x16x128_f8f6f4 v[94:97], v[18:25], v[176:183], 0
	v_mfma_f32_16x16x128_f8f6f4 v[90:93], v[26:33], v[176:183], 0
	s_waitcnt lgkmcnt(4)
	v_mfma_f32_16x16x128_f8f6f4 v[78:81], v[18:25], v[184:191], 0
	v_mfma_f32_16x16x128_f8f6f4 v[74:77], v[26:33], v[184:191], 0
	s_waitcnt lgkmcnt(2)
	v_mfma_f32_16x16x128_f8f6f4 v[62:65], v[18:25], v[192:199], 0
	v_mfma_f32_16x16x128_f8f6f4 v[58:61], v[26:33], v[192:199], 0
	s_waitcnt lgkmcnt(0)
	v_mfma_f32_16x16x128_f8f6f4 v[46:49], v[18:25], v[200:207], 0
	v_mfma_f32_16x16x128_f8f6f4 v[42:45], v[26:33], v[200:207], 0
	s_setprio 0
	s_setprio 1
	v_mfma_f32_16x16x128_f8f6f4 v[86:89], v[2:9], v[176:183], 0
	v_mfma_f32_16x16x128_f8f6f4 v[82:85], v[10:17], v[176:183], 0
	v_mfma_f32_16x16x128_f8f6f4 v[70:73], v[2:9], v[184:191], 0
	v_mfma_f32_16x16x128_f8f6f4 v[66:69], v[10:17], v[184:191], 0
	v_mfma_f32_16x16x128_f8f6f4 v[54:57], v[2:9], v[192:199], 0
	v_mfma_f32_16x16x128_f8f6f4 v[50:53], v[10:17], v[192:199], 0
	v_mfma_f32_16x16x128_f8f6f4 v[38:41], v[2:9], v[200:207], 0
	v_mfma_f32_16x16x128_f8f6f4 v[34:37], v[10:17], v[200:207], 0
	s_setprio 0
	s_barrier
	s_branch .Lmid7
